# v037 + non-temporal hint on the P18 f32 output stores
# speedup vs baseline: 1.0070x; 1.0012x over previous
.LBB0_3228:
	s_add_i32 s10, s8, -3
	s_ashr_i32 s11, s10, 31
	s_lshl_b64 s[10:11], s[10:11], 2
	s_add_u32 s14, s74, s10
	s_addc_u32 s15, s75, s11
	s_add_u32 s10, s76, s10
	s_addc_u32 s11, s77, s11
	global_load_dword v1, v17, s[14:15]
	global_load_dword v0, v17, s[10:11]
	s_add_i32 s10, s8, -2
	s_ashr_i32 s11, s10, 31
	s_lshl_b64 s[10:11], s[10:11], 2
	s_add_u32 s14, s74, s10
	s_addc_u32 s15, s75, s11
	s_add_u32 s10, s76, s10
	s_addc_u32 s11, s77, s11
	global_load_dword v3, v17, s[14:15]
	global_load_dword v2, v17, s[10:11]
	s_add_i32 s14, s8, -1
	s_ashr_i32 s15, s14, 31
	s_lshl_b64 s[10:11], s[14:15], 2
	s_add_u32 s14, s74, s10
	s_addc_u32 s15, s75, s11
	s_add_u32 s10, s76, s10
	global_load_dword v5, v17, s[14:15]
	s_addc_u32 s11, s77, s11
	s_ashr_i32 s9, s8, 31
	global_load_dword v4, v17, s[10:11]
	s_lshl_b64 s[10:11], s[8:9], 2
	s_add_u32 s14, s74, s10
	s_addc_u32 s15, s75, s11
	global_load_dword v7, v17, s[14:15]
	s_add_u32 s10, s76, s10
	s_addc_u32 s11, s77, s11
	global_load_dword v6, v17, s[10:11]
	global_load_dwordx2 v[8:9], v[18:19], off
	global_load_dwordx2 v[10:11], v[18:19], off offset:512
	global_load_dwordx2 v[12:13], v[18:19], off offset:1024
	global_load_dwordx2 v[14:15], v[18:19], off offset:1536
	s_and_b64 vcc, exec, s[0:1]
	s_waitcnt vmcnt(11)
	v_lshlrev_b32_e32 v1, 2, v1
	v_add_u32_e32 v16, s3, v1
	ds_read_b32 v40, v16
	s_waitcnt vmcnt(10)
	v_ashrrev_i32_e32 v1, 31, v0
	v_lshlrev_b64 v[0:1], 10, v[0:1]
	s_waitcnt vmcnt(9)
	v_lshlrev_b32_e32 v3, 2, v3
	v_add_u32_e32 v3, s3, v3
	ds_read_b32 v42, v3
	s_waitcnt lgkmcnt(1)
	v_ashrrev_i32_e32 v41, 31, v40
	v_lshlrev_b64 v[40:41], 18, v[40:41]
	v_lshl_add_u64 v[40:41], s[92:93], 0, v[40:41]
	v_lshl_add_u64 v[0:1], v[40:41], 0, v[0:1]
	s_waitcnt vmcnt(8)
	v_ashrrev_i32_e32 v3, 31, v2
	v_readfirstlane_b32 s10, v0
	v_readfirstlane_b32 s11, v1
	v_lshlrev_b64 v[0:1], 10, v[2:3]
	s_waitcnt vmcnt(7)
	v_lshlrev_b32_e32 v2, 2, v5
	v_add_u32_e32 v2, s3, v2
	s_waitcnt lgkmcnt(0)
	v_ashrrev_i32_e32 v43, 31, v42
	global_load_dword v16, v38, s[10:11]
	global_load_dword v39, v38, s[10:11] offset:256
	ds_read_b32 v2, v2
	v_lshlrev_b64 v[40:41], 18, v[42:43]
	v_lshl_add_u64 v[40:41], s[92:93], 0, v[40:41]
	v_lshl_add_u64 v[0:1], v[40:41], 0, v[0:1]
	s_waitcnt vmcnt(7)
	v_lshlrev_b32_e32 v3, 2, v7
	global_load_dword v50, v38, s[10:11] offset:512
	global_load_dword v54, v38, s[10:11] offset:768
	v_readfirstlane_b32 s10, v0
	v_readfirstlane_b32 s11, v1
	v_ashrrev_i32_e32 v5, 31, v4
	v_add_u32_e32 v3, s3, v3
	s_nop 2
	global_load_dword v58, v38, s[10:11]
	global_load_dword v62, v38, s[10:11] offset:256
	v_lshlrev_b64 v[0:1], 10, v[4:5]
	ds_read_b32 v4, v3
	s_waitcnt lgkmcnt(1)
	v_ashrrev_i32_e32 v3, 31, v2
	global_load_dword v66, v38, s[10:11] offset:512
	global_load_dword v70, v38, s[10:11] offset:768
	v_lshlrev_b64 v[2:3], 18, v[2:3]
	v_lshl_add_u64 v[2:3], s[92:93], 0, v[2:3]
	v_lshl_add_u64 v[0:1], v[2:3], 0, v[0:1]
	s_waitcnt lgkmcnt(0)
	v_ashrrev_i32_e32 v5, 31, v4
	v_readfirstlane_b32 s10, v0
	v_readfirstlane_b32 s11, v1
	s_nop 4
	global_load_dword v72, v38, s[10:11]
	global_load_dword v73, v38, s[10:11] offset:256
	global_load_dword v74, v38, s[10:11] offset:512
	global_load_dword v75, v38, s[10:11] offset:768
	s_waitcnt vmcnt(16)
	v_ashrrev_i32_e32 v7, 31, v6
	v_lshlrev_b64 v[2:3], 18, v[4:5]
	v_lshlrev_b64 v[0:1], 10, v[6:7]
	v_lshl_add_u64 v[2:3], s[92:93], 0, v[2:3]
	v_lshl_add_u64 v[0:1], v[2:3], 0, v[0:1]
	s_waitcnt vmcnt(15)
	v_lshlrev_b32_e32 v2, 16, v9
	v_readfirstlane_b32 s10, v0
	v_readfirstlane_b32 s11, v1
	s_nop 4
	global_load_dword v76, v38, s[10:11]
	global_load_dword v77, v38, s[10:11] offset:256
	global_load_dword v78, v38, s[10:11] offset:512
	global_load_dword v79, v38, s[10:11] offset:768
	v_lshlrev_b32_e32 v0, 16, v8
	v_and_b32_e32 v1, 0xffff0000, v8
	v_and_b32_e32 v3, 0xffff0000, v9
	s_waitcnt vmcnt(18)
	v_lshlrev_b32_e32 v4, 16, v10
	v_and_b32_e32 v5, 0xffff0000, v10
	v_lshlrev_b32_e32 v6, 16, v11
	v_and_b32_e32 v7, 0xffff0000, v11
	s_waitcnt vmcnt(17)
	v_lshlrev_b32_e32 v40, 16, v12
	v_and_b32_e32 v41, 0xffff0000, v12
	v_lshlrev_b32_e32 v42, 16, v13
	v_and_b32_e32 v43, 0xffff0000, v13
	s_waitcnt vmcnt(16)
	v_lshlrev_b32_e32 v44, 16, v14
	v_and_b32_e32 v45, 0xffff0000, v14
	v_lshlrev_b32_e32 v46, 16, v15
	v_and_b32_e32 v47, 0xffff0000, v15
	s_waitcnt vmcnt(15)
	v_cvt_pk_f32_fp8_e32 v[8:9], v16
	v_cvt_pk_f32_fp8_sdwa v[10:11], v16 src0_sel:WORD_1
	s_waitcnt vmcnt(14)
	v_cvt_pk_f32_fp8_e32 v[12:13], v39
	v_cvt_pk_f32_fp8_sdwa v[14:15], v39 src0_sel:WORD_1
	v_pk_add_f32 v[8:9], v[8:9], 0 op_sel_hi:[1,0]
	v_pk_add_f32 v[10:11], v[10:11], 0 op_sel_hi:[1,0]
	v_pk_add_f32 v[12:13], v[12:13], 0 op_sel_hi:[1,0]
	s_waitcnt vmcnt(13)
	v_cvt_pk_f32_fp8_e32 v[48:49], v50
	v_cvt_pk_f32_fp8_sdwa v[50:51], v50 src0_sel:WORD_1
	s_waitcnt vmcnt(12)
	v_cvt_pk_f32_fp8_e32 v[52:53], v54
	v_cvt_pk_f32_fp8_sdwa v[54:55], v54 src0_sel:WORD_1
	v_pk_add_f32 v[14:15], v[14:15], 0 op_sel_hi:[1,0]
	s_waitcnt vmcnt(11)
	v_cvt_pk_f32_fp8_e32 v[56:57], v58
	v_cvt_pk_f32_fp8_sdwa v[58:59], v58 src0_sel:WORD_1
	s_waitcnt vmcnt(10)
	v_cvt_pk_f32_fp8_e32 v[60:61], v62
	v_cvt_pk_f32_fp8_sdwa v[62:63], v62 src0_sel:WORD_1
	v_pk_add_f32 v[50:51], v[50:51], 0 op_sel_hi:[1,0]
	s_waitcnt vmcnt(9)
	v_cvt_pk_f32_fp8_e32 v[64:65], v66
	v_cvt_pk_f32_fp8_sdwa v[66:67], v66 src0_sel:WORD_1
	s_waitcnt vmcnt(8)
	v_cvt_pk_f32_fp8_e32 v[68:69], v70
	v_cvt_pk_f32_fp8_sdwa v[70:71], v70 src0_sel:WORD_1
	v_pk_add_f32 v[48:49], v[48:49], 0 op_sel_hi:[1,0]
	v_pk_add_f32 v[54:55], v[54:55], 0 op_sel_hi:[1,0]
	v_pk_add_f32 v[52:53], v[52:53], 0 op_sel_hi:[1,0]
	v_pk_add_f32 v[8:9], v[8:9], v[56:57]
	v_pk_add_f32 v[10:11], v[10:11], v[58:59]
	v_pk_add_f32 v[12:13], v[12:13], v[60:61]
	v_pk_add_f32 v[14:15], v[14:15], v[62:63]
	v_pk_add_f32 v[48:49], v[48:49], v[64:65]
	v_pk_add_f32 v[50:51], v[50:51], v[66:67]
	v_pk_add_f32 v[52:53], v[52:53], v[68:69]
	v_pk_add_f32 v[54:55], v[54:55], v[70:71]
	s_waitcnt vmcnt(7)
	v_cvt_pk_f32_fp8_e32 v[56:57], v72
	v_cvt_pk_f32_fp8_sdwa v[58:59], v72 src0_sel:WORD_1
	s_waitcnt vmcnt(6)
	v_cvt_pk_f32_fp8_e32 v[60:61], v73
	v_cvt_pk_f32_fp8_sdwa v[62:63], v73 src0_sel:WORD_1
	s_waitcnt vmcnt(5)
	v_cvt_pk_f32_fp8_e32 v[64:65], v74
	v_cvt_pk_f32_fp8_sdwa v[66:67], v74 src0_sel:WORD_1
	s_waitcnt vmcnt(4)
	v_cvt_pk_f32_fp8_e32 v[68:69], v75
	v_cvt_pk_f32_fp8_sdwa v[70:71], v75 src0_sel:WORD_1
	v_pk_add_f32 v[10:11], v[10:11], v[58:59]
	v_pk_add_f32 v[8:9], v[8:9], v[56:57]
	v_pk_add_f32 v[14:15], v[14:15], v[62:63]
	v_pk_add_f32 v[12:13], v[12:13], v[60:61]
	v_pk_add_f32 v[50:51], v[50:51], v[66:67]
	v_pk_add_f32 v[48:49], v[48:49], v[64:65]
	v_pk_add_f32 v[54:55], v[54:55], v[70:71]
	v_pk_add_f32 v[52:53], v[52:53], v[68:69]
	s_waitcnt vmcnt(3)
	v_cvt_pk_f32_fp8_e32 v[56:57], v76
	v_cvt_pk_f32_fp8_sdwa v[58:59], v76 src0_sel:WORD_1
	s_waitcnt vmcnt(2)
	v_cvt_pk_f32_fp8_e32 v[60:61], v77
	v_cvt_pk_f32_fp8_sdwa v[62:63], v77 src0_sel:WORD_1
	s_waitcnt vmcnt(1)
	v_cvt_pk_f32_fp8_e32 v[64:65], v78
	v_cvt_pk_f32_fp8_sdwa v[66:67], v78 src0_sel:WORD_1
	s_waitcnt vmcnt(0)
	v_cvt_pk_f32_fp8_e32 v[68:69], v79
	v_cvt_pk_f32_fp8_sdwa v[70:71], v79 src0_sel:WORD_1
	v_pk_add_f32 v[8:9], v[8:9], v[56:57]
	v_pk_add_f32 v[10:11], v[10:11], v[58:59]
	v_pk_add_f32 v[56:57], v[12:13], v[60:61]
	v_pk_add_f32 v[58:59], v[14:15], v[62:63]
	v_pk_add_f32 v[48:49], v[48:49], v[64:65]
	v_pk_add_f32 v[50:51], v[50:51], v[66:67]
	v_pk_add_f32 v[52:53], v[52:53], v[68:69]
	v_pk_add_f32 v[54:55], v[54:55], v[70:71]
	v_pk_fma_f32 v[14:15], v[30:31], v[10:11], v[2:3]
	v_pk_fma_f32 v[12:13], v[32:33], v[8:9], v[0:1]
	v_pk_fma_f32 v[10:11], v[22:23], v[58:59], v[6:7]
	v_pk_fma_f32 v[8:9], v[24:25], v[56:57], v[4:5]
	v_pk_fma_f32 v[6:7], v[26:27], v[50:51], v[42:43]
	v_pk_fma_f32 v[4:5], v[28:29], v[48:49], v[40:41]
	v_pk_fma_f32 v[2:3], v[34:35], v[54:55], v[46:47]
	v_pk_fma_f32 v[0:1], v[36:37], v[52:53], v[44:45]
	s_cbranch_vccnz .LBB0_3230
	global_store_dwordx4 v[20:21], v[12:15], off offset:-3072 nt
	global_store_dwordx4 v[20:21], v[8:11], off offset:-2048 nt
	global_store_dwordx4 v[20:21], v[4:7], off offset:-1024 nt
	global_store_dwordx4 v[20:21], v[0:3], off nt
	s_cbranch_execnz .LBB0_3227
	s_branch .LBB0_3231
